# BG_CONV 93 (11 in-proj rounds), P5 weight loads hoisted above stores, P7 x1 row loads batched + token-1 prefetch
# speedup vs baseline: 1.0164x; 1.0164x over previous
.LBB0_8:
	s_load_dwordx16 s[52:67], s[0:1], 0x0
	s_load_dwordx16 s[36:51], s[0:1], 0x40
	s_and_b64 s[0:1], s[80:81], exec
	s_cselect_b32 s3, 0x5d, 0
	s_cmp_lt_i32 s2, s3
	s_cselect_b64 s[30:31], -1, 0
	s_cmp_ge_i32 s2, s3
	s_cselect_b64 s[26:27], -1, 0
	s_xor_b64 s[0:1], s[80:81], -1
	s_or_b64 s[0:1], s[30:31], s[0:1]
	s_sub_i32 s24, s33, s3
	s_and_b64 vcc, exec, s[0:1]
	s_cbranch_vccnz .LBB0_13
	s_add_u32 s28, s76, 0x3600
	s_getreg_b32 s0, hwreg(HW_REG_XCC_ID, 0, 4)
	s_addc_u32 s29, s77, 0
	s_and_b32 s88, s0, 15
	v_cmp_eq_u32_e32 vcc, 0, v0
	s_and_saveexec_b64 s[0:1], vcc
	s_cbranch_execz .LBB0_12
	s_mov_b64 s[6:7], exec
	v_mbcnt_lo_u32_b32 v1, s6, 0
	v_mbcnt_hi_u32_b32 v1, s7, v1
	v_cmp_eq_u32_e32 vcc, 0, v1
	s_and_b64 s[8:9], exec, vcc
	s_mov_b64 exec, s[8:9]
	s_cbranch_execz .LBB0_12
	s_lshl_b32 s8, s88, 8
	s_bcnt1_i32_b64 s6, s[6:7]
	v_mov_b32_e32 v1, s8
	v_mov_b32_e32 v2, s6
	global_atomic_add v1, v2, s[28:29] offset:1024

.LBB0_184:
	s_and_b64 s[6:7], s[80:81], exec
	s_cselect_b32 s21, 0x5d, s33
	s_add_i32 s12, s21, s2
	s_cmpk_gt_i32 s12, 0x5fff
	s_cbranch_scc1 .LBB0_187
	s_cmpk_gt_i32 s12, 0x3fff
	s_cbranch_scc0 .LBB0_190
	s_add_i32 s6, s12, 0xffffc000
	s_lshr_b32 s6, s6, 8
	s_mov_b32 s7, 0
	s_bfe_u32 s13, s12, 0x40004
	s_lshl_b64 s[8:9], s[6:7], 24
	s_waitcnt lgkmcnt(0)
	v_readlane_b32 s64, v254, 0
	v_readlane_b32 s65, v254, 1
	s_add_u32 s8, s64, s8
	s_addc_u32 s9, s65, s9
	s_lshl_b32 s10, s13, 20
	s_add_u32 s8, s8, s10
	s_addc_u32 s9, s9, 0
	s_lshl_b32 s10, s12, 7
	s_and_b32 s14, s10, 0x780
	s_lshl_b32 s10, s14, 2
	s_add_u32 s10, s8, s10
	s_addc_u32 s11, s9, 0
	s_lshl_b64 s[6:7], s[6:7], 22
	s_lshl_b32 s8, s14, 11
	s_add_u32 s6, s76, s6
	s_addc_u32 s7, s77, s7
	s_add_u32 s6, s6, s8
	s_addc_u32 s7, s7, 0
	s_lshl_b32 s8, s13, 7
	s_add_u32 s6, s6, s8
	s_addc_u32 s7, s7, 0
	s_add_u32 s6, s6, 0x224e8000
	v_readlane_b32 s66, v254, 2
	v_readlane_b32 s67, v254, 3
	v_readlane_b32 s68, v254, 4
	v_readlane_b32 s69, v254, 5
	v_readlane_b32 s70, v254, 6
	v_readlane_b32 s71, v254, 7
	s_addc_u32 s7, s7, 0
	s_mov_b64 s[8:9], 0x800
	s_cbranch_execz .LBB0_191
	s_branch .LBB0_192

.LBB0_532:
	s_or_b64 exec, exec, s[82:83]
	s_lshl_b32 s82, s84, 2
	s_add_u32 s84, s40, s82
	s_addc_u32 s85, s41, 0
	v_lshlrev_b32_e32 v45, 2, v86
	s_waitcnt lgkmcnt(0)
	s_barrier
	global_load_dwordx4 v[66:69], v45, s[84:85]
	s_mov_b32 s83, s43
	global_load_dwordx4 v[194:197], v45, s[84:85] offset:64
	global_load_dwordx4 v[198:201], v45, s[84:85] offset:128
	v_lshlrev_b32_e32 v206, 2, v88
	global_load_dwordx4 v[202:205], v206, s[84:85]
	v_lshl_add_u64 v[208:209], v[90:91], 0, s[82:83]
	global_load_dwordx4 v[210:213], v[208:209], off
	global_load_dwordx4 v[214:217], v[208:209], off offset:16
	global_load_dwordx4 v[218:221], v[208:209], off offset:32
	global_load_dwordx4 v[222:225], v[208:209], off offset:48
	ds_read_b64 v[42:43], v115
	v_mad_u64_u32 v[46:47], vcc, v108, s74, v[110:111]
	v_mov_b32_e32 v154, v63
	v_mov_b32_e32 v155, v64
	v_mov_b32_e32 v63, v65
	v_lshlrev_b32_e32 v110, 16, v112
	v_mov_b32_e32 v64, v60
	v_mov_b32_e32 v65, v58
	v_mov_b32_e32 v58, v61
	v_mov_b32_e32 v60, v47
	v_pk_add_f32 v[62:63], v[154:155], v[62:63]
	v_mul_f32_e32 v47, 0xbfb8aa3b, v110
	v_pk_add_f32 v[58:59], v[64:65], v[58:59]
	v_mad_u64_u32 v[60:61], vcc, v9, s74, v[60:61]
	v_pk_add_f32 v[62:63], v[62:63], v[62:63] op_sel:[0,1] op_sel_hi:[1,0]
	v_exp_f32_e32 v9, v47
	v_sub_u32_e32 v47, v60, v108
	v_pk_add_f32 v[60:61], v[62:63], v[58:59] op_sel:[0,1] op_sel_hi:[1,0]
	s_waitcnt lgkmcnt(0)
	v_mov_b32_e32 v59, v42
	v_mov_b32_e32 v61, v43
	v_lshlrev_b32_e32 v148, 16, v113
	v_pk_add_f32 v[42:43], v[58:59], v[60:61]
	v_and_b32_e32 v112, 0xffff0000, v112
	v_and_b32_e32 v150, 0xffff0000, v113
	v_mul_f32_e32 v111, 0xbfb8aa3b, v148
	v_lshl_add_u64 v[46:47], v[46:47], 0, s[42:43]
	s_mov_b64 vcc, 0x8688b800
	v_pk_fma_f32 v[42:43], v[42:43], s[66:67], v[98:99] op_sel_hi:[1,1,0]
	v_mul_f32_e32 v97, 0xbfb8aa3b, v112
	v_mul_f32_e32 v113, 0xbfb8aa3b, v150
	v_exp_f32_e32 v65, v111
	v_lshl_add_u64 v[46:47], v[46:47], 0, vcc
	v_mul_f32_e32 v58, 0x4b800000, v43
	v_cmp_gt_f32_e32 vcc, s75, v43
	v_exp_f32_e32 v64, v97
	v_exp_f32_e32 v97, v113
	v_cndmask_b32_e32 v43, v43, v58, vcc
	v_rsq_f32_e32 v43, v43
	v_add_f32_e32 v9, 1.0, v9
	v_add_f32_e32 v62, 1.0, v65
	v_add_f32_e32 v63, 1.0, v64
	v_add_f32_e32 v64, 1.0, v97
	v_rcp_f32_e32 v60, v9
	v_rcp_f32_e32 v62, v62
	v_mul_f32_e32 v9, 0x45800000, v43
	v_cndmask_b32_e32 v9, v43, v9, vcc
	v_mul_f32_e32 v111, v38, v9
	v_mul_f32_e32 v149, v40, v9
	v_mul_f32_e32 v113, v39, v9
	v_mul_f32_e32 v151, v41, v9
	v_lshlrev_b32_e32 v152, 1, v86
	v_mov_b32_e32 v153, v75
	v_lshl_add_u64 v[58:59], v[46:47], 0, v[152:153]
	s_mov_b32 s83, s43
	v_cmp_gt_f32_e32 vcc, s75, v42
	s_waitcnt vmcnt(7)
	v_mov_b32_e32 v61, v66
	v_rcp_f32_e32 v66, v63
	v_mov_b32_e32 v63, v68
	v_rcp_f32_e32 v68, v64
	v_pk_mul_f32 v[38:39], v[60:61], v[110:111]
	v_pk_mul_f32 v[40:41], v[62:63], v[148:149]
	v_mul_f32_e32 v43, v38, v39
	v_mul_f32_e32 v60, v40, v41
	v_pk_mul_f32 v[38:39], v[66:67], v[112:113]
	v_pk_mul_f32 v[40:41], v[68:69], v[150:151]
	v_mul_f32_e32 v38, v38, v39
	v_mul_f32_e32 v39, v40, v41
	v_cvt_pk_bf16_f32 v38, v43, v38
	v_cvt_pk_bf16_f32 v39, v60, v39
	global_store_dwordx2 v[58:59], v[38:39], off
	v_lshlrev_b32_e32 v60, 16, v106
	v_and_b32_e32 v62, 0xffff0000, v106
	v_lshlrev_b32_e32 v64, 16, v107
	v_and_b32_e32 v66, 0xffff0000, v107
	v_mul_f32_e32 v43, 0xbfb8aa3b, v60
	v_mul_f32_e32 v61, 0xbfb8aa3b, v62
	v_mul_f32_e32 v63, 0xbfb8aa3b, v64
	v_mul_f32_e32 v65, 0xbfb8aa3b, v66
	v_exp_f32_e32 v43, v43
	v_exp_f32_e32 v61, v61
	v_exp_f32_e32 v63, v63
	v_exp_f32_e32 v65, v65
	v_add_f32_e32 v43, 1.0, v43
	v_add_f32_e32 v61, 1.0, v61
	v_add_f32_e32 v63, 1.0, v63
	v_add_f32_e32 v65, 1.0, v65
	v_rcp_f32_e32 v68, v43
	v_rcp_f32_e32 v106, v61
	v_rcp_f32_e32 v110, v63
	v_rcp_f32_e32 v112, v65
	v_mul_f32_e32 v61, v34, v9
	v_mul_f32_e32 v63, v35, v9
	v_mul_f32_e32 v65, v36, v9
	v_mul_f32_e32 v67, v37, v9
	v_lshlrev_b32_e32 v43, 2, v88
	s_waitcnt vmcnt(7)
	v_mov_b32_e32 v69, v194
	v_mov_b32_e32 v107, v195
	v_mov_b32_e32 v111, v196
	v_mov_b32_e32 v113, v197
	v_pk_mul_f32 v[34:35], v[68:69], v[60:61]
	v_pk_mul_f32 v[36:37], v[106:107], v[62:63]
	v_pk_mul_f32 v[38:39], v[110:111], v[64:65]
	v_pk_mul_f32 v[40:41], v[112:113], v[66:67]
	v_mul_f32_e32 v34, v34, v35
	v_mul_f32_e32 v35, v36, v37
	v_mul_f32_e32 v36, v38, v39
	v_mul_f32_e32 v37, v40, v41
	v_cvt_pk_bf16_f32 v34, v34, v35
	v_cvt_pk_bf16_f32 v35, v36, v37
	global_store_dwordx2 v[58:59], v[34:35], off offset:32
	v_lshlrev_b32_e32 v38, 16, v104
	v_and_b32_e32 v40, 0xffff0000, v104
	v_lshlrev_b32_e32 v60, 16, v105
	v_and_b32_e32 v62, 0xffff0000, v105
	v_mul_f32_e32 v39, 0xbfb8aa3b, v38
	v_mul_f32_e32 v41, 0xbfb8aa3b, v40
	v_mul_f32_e32 v45, 0xbfb8aa3b, v60
	v_mul_f32_e32 v61, 0xbfb8aa3b, v62
	v_exp_f32_e32 v39, v39
	v_exp_f32_e32 v41, v41
	v_exp_f32_e32 v45, v45
	v_exp_f32_e32 v61, v61
	v_add_f32_e32 v39, 1.0, v39
	v_add_f32_e32 v41, 1.0, v41
	v_add_f32_e32 v45, 1.0, v45
	v_add_f32_e32 v61, 1.0, v61
	v_rcp_f32_e32 v64, v39
	v_rcp_f32_e32 v66, v41
	v_rcp_f32_e32 v68, v45
	v_rcp_f32_e32 v104, v61
	v_mul_f32_e32 v65, v30, v9
	v_mul_f32_e32 v67, v31, v9
	v_mul_f32_e32 v69, v32, v9
	v_mul_f32_e32 v105, v33, v9
	v_and_b32_e32 v45, 0xffff0000, v54
	s_waitcnt vmcnt(7)
	v_mov_b32_e32 v39, v198
	v_mov_b32_e32 v41, v199
	v_mov_b32_e32 v61, v200
	v_mov_b32_e32 v63, v201
	v_pk_mul_f32 v[30:31], v[64:65], v[38:39]
	v_pk_mul_f32 v[32:33], v[66:67], v[40:41]
	v_pk_mul_f32 v[34:35], v[68:69], v[60:61]
	v_pk_mul_f32 v[36:37], v[104:105], v[62:63]
	v_mul_f32_e32 v30, v30, v31
	v_mul_f32_e32 v31, v32, v33
	v_mul_f32_e32 v32, v34, v35
	v_mul_f32_e32 v33, v36, v37
	v_cvt_pk_bf16_f32 v30, v30, v31
	v_cvt_pk_bf16_f32 v31, v32, v33
	global_store_dwordx2 v[58:59], v[30:31], off offset:64
	v_lshlrev_b32_e32 v34, 16, v102
	v_and_b32_e32 v36, 0xffff0000, v102
	v_lshlrev_b32_e32 v38, 16, v103
	v_and_b32_e32 v40, 0xffff0000, v103
	v_mul_f32_e32 v35, 0xbfb8aa3b, v34
	v_mul_f32_e32 v37, 0xbfb8aa3b, v36
	v_mul_f32_e32 v39, 0xbfb8aa3b, v38
	v_mul_f32_e32 v41, 0xbfb8aa3b, v40
	v_exp_f32_e32 v35, v35
	v_exp_f32_e32 v37, v37
	v_exp_f32_e32 v39, v39
	v_exp_f32_e32 v41, v41
	v_lshlrev_b32_e32 v58, 1, v88
	v_mov_b32_e32 v59, v75
	v_add_f32_e32 v35, 1.0, v35
	v_add_f32_e32 v37, 1.0, v37
	v_add_f32_e32 v39, 1.0, v39
	v_add_f32_e32 v41, 1.0, v41
	v_lshl_add_u64 v[46:47], v[46:47], 0, v[58:59]
	v_rcp_f32_e32 v58, v35
	v_rcp_f32_e32 v62, v37
	v_rcp_f32_e32 v64, v39
	v_rcp_f32_e32 v66, v41
	v_mul_f32_e32 v59, v26, v9
	v_mul_f32_e32 v63, v27, v9
	v_mul_f32_e32 v65, v28, v9
	v_mul_f32_e32 v67, v29, v9
	v_lshl_add_u64 v[60:61], v[90:91], 0, s[82:83]
	v_mul_f32_e32 v43, 0x4b800000, v42
	v_cndmask_b32_e32 v42, v42, v43, vcc
	s_waitcnt vmcnt(7)
	v_mov_b32_e32 v35, v202
	v_mov_b32_e32 v37, v203
	v_mov_b32_e32 v39, v204
	v_mov_b32_e32 v41, v205
	v_pk_mul_f32 v[26:27], v[58:59], v[34:35]
	v_pk_mul_f32 v[28:29], v[62:63], v[36:37]
	v_pk_mul_f32 v[30:31], v[64:65], v[38:39]
	v_pk_mul_f32 v[32:33], v[66:67], v[40:41]
	v_mul_f32_e32 v9, v26, v27
	v_mul_f32_e32 v26, v28, v29
	v_mul_f32_e32 v27, v30, v31
	v_mul_f32_e32 v28, v32, v33
	v_cvt_pk_bf16_f32 v26, v9, v26
	v_cvt_pk_bf16_f32 v27, v27, v28
	global_store_dwordx2 v[46:47], v[26:27], off
	v_rsq_f32_e32 v64, v42
	v_lshlrev_b64 v[46:47], 11, v[100:101]
	v_lshl_add_u64 v[46:47], v[46:47], 1, s[36:37]
	v_lshl_add_u64 v[46:47], v[46:47], 0, s[42:43]
	v_lshl_add_u64 v[42:43], v[46:47], 0, v[74:75]
	v_mul_f32_e32 v46, 0x45800000, v64
	v_cndmask_b32_e32 v46, v64, v46, vcc
	v_lshlrev_b32_e32 v9, 16, v54
	v_lshlrev_b32_e32 v54, 16, v55
	v_and_b32_e32 v55, 0xffff0000, v55
	v_lshlrev_b32_e32 v58, 16, v56
	v_and_b32_e32 v56, 0xffff0000, v56
	v_lshlrev_b32_e32 v59, 16, v57
	v_and_b32_e32 v57, 0xffff0000, v57
	v_lshlrev_b32_e32 v60, 16, v50
	s_and_b32 s42, s91, 7
	v_and_b32_e32 v50, 0xffff0000, v50
	v_lshlrev_b32_e32 v61, 16, v51
	v_and_b32_e32 v51, 0xffff0000, v51
	v_lshlrev_b32_e32 v62, 16, v52
	v_and_b32_e32 v52, 0xffff0000, v52
	v_lshlrev_b32_e32 v63, 16, v53
	v_and_b32_e32 v53, 0xffff0000, v53
	s_cmp_lg_u32 s42, 7
	s_waitcnt vmcnt(7)
	v_pk_mul_f32 v[28:29], v[46:47], v[212:213] op_sel_hi:[0,1]
	v_pk_mul_f32 v[26:27], v[46:47], v[210:211] op_sel_hi:[0,1]
	s_waitcnt vmcnt(6)
	v_pk_mul_f32 v[30:31], v[46:47], v[214:215] op_sel_hi:[0,1]
	v_pk_mul_f32 v[32:33], v[46:47], v[216:217] op_sel_hi:[0,1]
	s_waitcnt vmcnt(5)
	v_pk_mul_f32 v[34:35], v[46:47], v[218:219] op_sel_hi:[0,1]
	v_mul_f32_e32 v9, v26, v9
	v_mul_f32_e32 v26, v27, v45
	v_mul_f32_e32 v27, v28, v54
	v_mul_f32_e32 v28, v29, v55
	v_mul_f32_e32 v29, v30, v58
	v_pk_mul_f32 v[36:37], v[46:47], v[220:221] op_sel_hi:[0,1]
	s_waitcnt vmcnt(4)
	v_pk_mul_f32 v[40:41], v[46:47], v[224:225] op_sel_hi:[0,1]
	v_pk_mul_f32 v[38:39], v[46:47], v[222:223] op_sel_hi:[0,1]
	v_mul_f32_e32 v30, v31, v56
	v_mul_f32_e32 v31, v32, v59
	v_mul_f32_e32 v32, v33, v57
	v_mul_f32_e32 v33, v34, v60
	v_cvt_pk_bf16_f32 v26, v9, v26
	v_cvt_pk_bf16_f32 v27, v27, v28
	v_cvt_pk_bf16_f32 v28, v29, v30
	v_cvt_pk_bf16_f32 v29, v31, v32
	v_mul_f32_e32 v34, v35, v50
	v_mul_f32_e32 v35, v36, v61
	v_mul_f32_e32 v36, v37, v51
	v_mul_f32_e32 v37, v38, v62
	v_mul_f32_e32 v38, v39, v52
	v_mul_f32_e32 v39, v40, v63
	v_mul_f32_e32 v40, v41, v53
	v_cvt_pk_bf16_f32 v30, v33, v34
	v_cvt_pk_bf16_f32 v31, v35, v36
	v_cvt_pk_bf16_f32 v32, v37, v38
	v_cvt_pk_bf16_f32 v33, v39, v40
	global_store_dwordx4 v[42:43], v[26:29], off
	global_store_dwordx4 v[42:43], v[30:33], off offset:16
	s_barrier
	s_cbranch_scc1 .LBB0_523
	v_xor_b32_e32 v9, 8, v130
	v_cmp_lt_i32_e32 vcc, v9, v44
	v_xor_b32_e32 v26, 4, v130
	s_add_i32 s42, s94, s71
	v_cndmask_b32_e32 v9, v130, v9, vcc
	v_cmp_lt_i32_e32 vcc, v26, v44
	s_lshl_b64 s[82:83], s[80:81], 24
	s_lshl_b64 s[84:85], s[42:43], 11
	v_cndmask_b32_e32 v26, v130, v26, vcc
	v_lshlrev_b32_e32 v50, 2, v26
	v_xor_b32_e32 v26, 2, v130
	s_add_u32 s82, s84, s82
	v_cmp_lt_i32_e32 vcc, v26, v44
	s_addc_u32 s83, s85, s83
	v_lshl_add_u64 v[42:43], s[82:83], 0, v[92:93]
	v_cndmask_b32_e32 v26, v130, v26, vcc
	s_lshl_b64 s[82:83], s[80:81], 25
	s_lshl_b64 s[84:85], s[42:43], 12
	v_lshlrev_b32_e32 v51, 2, v26
	v_xor_b32_e32 v26, 1, v130
	s_add_u32 s61, s84, s82
	v_cmp_lt_i32_e32 vcc, v26, v44
	s_addc_u32 s65, s85, s83
	s_lshl_b64 s[80:81], s[80:81], 15
	s_lshl_b32 s42, s42, 2
	v_cndmask_b32_e32 v26, v130, v26, vcc
	s_add_u32 s42, s80, s42
	v_lshlrev_b32_e32 v9, 2, v9
	v_lshlrev_b32_e32 v52, 2, v26
	v_mov_b32_e32 v45, s65
	v_or_b32_e32 v44, s61, v94
	s_addc_u32 s61, s81, 0
	s_mov_b32 s65, -2
	s_branch .LBB0_535

.LBB0_682:
	v_lshl_add_u64 v[2:3], s[76:77], 0, v[28:29]
	v_add_co_u32_e32 v30, vcc, 0x54768000, v2
	s_add_i32 s22, s14, s15
	s_nop 0
	v_addc_co_u32_e32 v31, vcc, 0, v3, vcc
	global_load_dwordx2 v[226:227], v[30:31], off
	global_load_dwordx2 v[228:229], v[30:31], off offset:512
	global_load_dwordx2 v[230:231], v[30:31], off offset:1024
	global_load_dwordx2 v[232:233], v[30:31], off offset:1536
	global_load_dwordx2 v[234:235], v[30:31], off offset:2048
	global_load_dwordx2 v[236:237], v[30:31], off offset:2560
	global_load_dwordx2 v[238:239], v[30:31], off offset:3072
	global_load_dwordx2 v[240:241], v[30:31], off offset:3584
	s_add_i32 s98, s22, 1
	s_ashr_i32 s99, s98, 31
	s_lshl_b64 s[98:99], s[98:99], 12
	v_lshl_add_u64 v[252:253], v[22:23], 0, s[98:99]
	global_load_dwordx2 v[242:243], v[252:253], off
	global_load_dwordx2 v[244:245], v[252:253], off offset:512
	global_load_dwordx2 v[246:247], v[252:253], off offset:1024
	global_load_dwordx2 v[248:249], v[252:253], off offset:1536
	global_load_dwordx2 v[250:251], v[252:253], off offset:2048
	s_ashr_i32 s0, s22, 13
	s_mulk_i32 s0, 0x3000
	s_ashr_i32 s1, s0, 31
	s_lshl_b64 s[0:1], s[0:1], 2
	s_add_u32 s20, s3, s0
	s_addc_u32 s21, s24, s1
	s_add_u32 s0, s20, 0x6000
	s_addc_u32 s1, s21, 0
	s_add_u32 s20, s20, 0x8000
	s_addc_u32 s21, s21, 0
	s_waitcnt vmcnt(12)
	v_and_b32_e32 v3, 0xffff0000, v226
	s_waitcnt vmcnt(11)
	v_and_b32_e32 v57, 0xffff0000, v228
	v_lshlrev_b32_e32 v2, 16, v226
	v_mul_f32_e32 v34, v3, v3
	v_lshlrev_b32_e32 v56, 16, v228
	v_mul_f32_e32 v32, v57, v57
	v_lshlrev_b32_e32 v4, 16, v227
	v_fmac_f32_e32 v34, v2, v2
	v_lshlrev_b32_e32 v58, 16, v229
	v_fmac_f32_e32 v32, v56, v56
	v_and_b32_e32 v5, 0xffff0000, v227
	v_fmac_f32_e32 v34, v4, v4
	v_and_b32_e32 v59, 0xffff0000, v229
	v_fmac_f32_e32 v32, v58, v58
	v_fmac_f32_e32 v34, v5, v5
	v_fmac_f32_e32 v32, v59, v59
	v_add_f32_e32 v34, v34, v32
	s_waitcnt vmcnt(10)
	v_and_b32_e32 v53, 0xffff0000, v230
	v_lshlrev_b32_e32 v52, 16, v230
	v_mul_f32_e32 v32, v53, v53
	v_lshlrev_b32_e32 v54, 16, v231
	v_fmac_f32_e32 v32, v52, v52
	v_and_b32_e32 v55, 0xffff0000, v231
	v_fmac_f32_e32 v32, v54, v54
	v_fmac_f32_e32 v32, v55, v55
	v_add_f32_e32 v34, v34, v32
	s_waitcnt vmcnt(9)
	v_and_b32_e32 v49, 0xffff0000, v232
	v_lshlrev_b32_e32 v48, 16, v232
	v_mul_f32_e32 v32, v49, v49
	v_lshlrev_b32_e32 v50, 16, v233
	v_fmac_f32_e32 v32, v48, v48
	v_and_b32_e32 v51, 0xffff0000, v233
	v_fmac_f32_e32 v32, v50, v50
	v_fmac_f32_e32 v32, v51, v51
	v_add_f32_e32 v36, v34, v32
	s_waitcnt vmcnt(8)
	v_and_b32_e32 v42, 0xffff0000, v234
	s_waitcnt vmcnt(7)
	v_and_b32_e32 v43, 0xffff0000, v236
	v_lshlrev_b32_e32 v41, 16, v236
	v_lshlrev_b32_e32 v40, 16, v234
	v_lshlrev_b32_e32 v44, 16, v235
	v_and_b32_e32 v46, 0xffff0000, v235
	v_pk_mul_f32 v[32:33], v[42:43], v[42:43]
	v_lshlrev_b32_e32 v45, 16, v237
	v_pk_fma_f32 v[32:33], v[40:41], v[40:41], v[32:33]
	v_and_b32_e32 v47, 0xffff0000, v237
	v_pk_fma_f32 v[32:33], v[44:45], v[44:45], v[32:33]
	s_nop 0
	v_pk_fma_f32 v[32:33], v[46:47], v[46:47], v[32:33]
	s_nop 0
	v_add_f32_e32 v32, v36, v32
	global_load_dwordx4 v[214:217], v202, s[0:1]
	global_load_dwordx4 v[218:221], v202, s[20:21]
	global_load_dwordx4 v[222:225], v[8:9], off
	v_add_f32_e32 v38, v32, v33
	s_waitcnt vmcnt(9)
	v_and_b32_e32 v32, 0xffff0000, v238
	s_waitcnt vmcnt(8)
	v_and_b32_e32 v33, 0xffff0000, v240
	v_lshlrev_b32_e32 v31, 16, v240
	v_lshlrev_b32_e32 v30, 16, v238
	v_lshlrev_b32_e32 v34, 16, v239
	v_and_b32_e32 v36, 0xffff0000, v239
	v_pk_mul_f32 v[60:61], v[32:33], v[32:33]
	v_lshlrev_b32_e32 v35, 16, v241
	v_pk_fma_f32 v[60:61], v[30:31], v[30:31], v[60:61]
	v_and_b32_e32 v37, 0xffff0000, v241
	v_pk_fma_f32 v[60:61], v[34:35], v[34:35], v[60:61]
	s_waitcnt vmcnt(1)
	v_pk_add_f32 v[218:219], v[218:219], 1.0 op_sel_hi:[1,0]
	v_pk_fma_f32 v[60:61], v[36:37], v[36:37], v[60:61]
	s_nop 0
	v_add_f32_e32 v38, v38, v60
	v_add_f32_e32 v38, v38, v61
	ds_bpermute_b32 v60, v189, v38
	s_waitcnt lgkmcnt(0)
	v_add_f32_e32 v38, v38, v60
	ds_bpermute_b32 v60, v192, v38
	s_waitcnt lgkmcnt(0)
	v_add_f32_e32 v38, v38, v60
	ds_bpermute_b32 v60, v193, v38
	s_waitcnt lgkmcnt(0)
	v_add_f32_e32 v38, v38, v60
	ds_bpermute_b32 v60, v194, v38
	s_waitcnt lgkmcnt(0)
	v_add_f32_e32 v38, v38, v60
	ds_bpermute_b32 v60, v195, v38
	s_waitcnt lgkmcnt(0)
	v_add_f32_e32 v38, v38, v60
	ds_bpermute_b32 v60, v196, v38
	s_waitcnt lgkmcnt(0)
	v_add_f32_e32 v38, v38, v60
	v_fmamk_f32 v38, v38, 0x3a000000, v201
	v_cmp_gt_f32_e32 vcc, s27, v38
	v_mul_f32_e32 v60, 0x4b800000, v38
	s_nop 0
	v_cndmask_b32_e32 v38, v38, v60, vcc
	v_rsq_f32_e32 v38, v38
	s_nop 0
	v_mul_f32_e32 v60, 0x45800000, v38
	v_cndmask_b32_e32 v38, v38, v60, vcc
	v_pk_mul_f32 v[2:3], v[2:3], v[38:39] op_sel_hi:[1,0]
	v_pk_mul_f32 v[4:5], v[4:5], v[38:39] op_sel_hi:[1,0]
	s_waitcnt vmcnt(0)
	v_pk_mul_f32 v[2:3], v[222:223], v[2:3]
	v_pk_mul_f32 v[4:5], v[224:225], v[4:5]
	v_pk_fma_f32 v[2:3], v[218:219], v[2:3], v[214:215]
	v_mov_b32_e32 v214, 0
	v_cvt_pk_fp8_f32 v214, v2, v3
	v_pk_add_f32 v[60:61], v[220:221], 1.0 op_sel_hi:[1,0]
	v_pk_mul_f32 v[56:57], v[56:57], v[38:39] op_sel_hi:[1,0]
	v_pk_fma_f32 v[4:5], v[60:61], v[4:5], v[216:217]
	v_lshl_add_u64 v[60:61], s[76:77], 0, v[26:27]
	v_cvt_pk_fp8_f32 v214, v4, v5 op_sel:[0,0,1]
	v_add_co_u32_e32 v60, vcc, s28, v60
	ds_write_b128 v199, v[2:5]
	s_nop 0
	v_addc_co_u32_e32 v61, vcc, 0, v61, vcc
	global_store_dword v[60:61], v214, off
	global_load_dwordx4 v[2:5], v203, s[0:1]
	s_nop 0
	global_load_dwordx4 v[214:217], v203, s[20:21]
	global_load_dwordx4 v[218:221], v[8:9], off offset:1024
	v_pk_mul_f32 v[58:59], v[58:59], v[38:39] op_sel_hi:[1,0]
	v_pk_mul_f32 v[52:53], v[52:53], v[38:39] op_sel_hi:[1,0]
	v_pk_mul_f32 v[54:55], v[54:55], v[38:39] op_sel_hi:[1,0]
	v_pk_mul_f32 v[48:49], v[48:49], v[38:39] op_sel_hi:[1,0]
	v_pk_mul_f32 v[50:51], v[50:51], v[38:39] op_sel_hi:[1,0]
	s_waitcnt vmcnt(1)
	v_pk_add_f32 v[214:215], v[214:215], 1.0 op_sel_hi:[1,0]
	s_waitcnt vmcnt(0)
	v_pk_mul_f32 v[56:57], v[218:219], v[56:57]
	v_pk_mul_f32 v[58:59], v[220:221], v[58:59]
	v_pk_fma_f32 v[2:3], v[214:215], v[56:57], v[2:3]
	v_mov_b32_e32 v56, 0
	v_cvt_pk_fp8_f32 v56, v2, v3
	v_pk_add_f32 v[216:217], v[216:217], 1.0 op_sel_hi:[1,0]
	s_nop 0
	v_pk_fma_f32 v[4:5], v[216:217], v[58:59], v[4:5]
	ds_write_b128 v199, v[2:5] offset:1024
	v_cvt_pk_fp8_f32 v56, v4, v5 op_sel:[0,0,1]
	global_store_dword v[60:61], v56, off offset:256
	global_load_dwordx4 v[2:5], v204, s[0:1]
	s_nop 0
	global_load_dwordx4 v[56:59], v204, s[20:21]
	global_load_dwordx4 v[214:217], v[8:9], off offset:2048
	s_waitcnt vmcnt(1)
	v_pk_add_f32 v[56:57], v[56:57], 1.0 op_sel_hi:[1,0]
	s_waitcnt vmcnt(0)
	v_pk_mul_f32 v[52:53], v[214:215], v[52:53]
	v_pk_mul_f32 v[54:55], v[216:217], v[54:55]
	v_pk_fma_f32 v[2:3], v[56:57], v[52:53], v[2:3]
	v_mov_b32_e32 v52, 0
	v_cvt_pk_fp8_f32 v52, v2, v3
	v_pk_add_f32 v[58:59], v[58:59], 1.0 op_sel_hi:[1,0]
	s_nop 0
	v_pk_fma_f32 v[4:5], v[58:59], v[54:55], v[4:5]
	ds_write_b128 v199, v[2:5] offset:2048
	v_cvt_pk_fp8_f32 v52, v4, v5 op_sel:[0,0,1]
	global_store_dword v[60:61], v52, off offset:512
	global_load_dwordx4 v[2:5], v205, s[0:1]
	s_nop 0
	global_load_dwordx4 v[52:55], v205, s[20:21]
	global_load_dwordx4 v[56:59], v[8:9], off offset:3072
	s_waitcnt vmcnt(1)
	v_pk_add_f32 v[52:53], v[52:53], 1.0 op_sel_hi:[1,0]
	s_waitcnt vmcnt(0)
	v_pk_mul_f32 v[48:49], v[48:49], v[56:57]
	v_pk_mul_f32 v[50:51], v[50:51], v[58:59]
	v_pk_fma_f32 v[2:3], v[52:53], v[48:49], v[2:3]
	v_mov_b32_e32 v48, 0
	v_cvt_pk_fp8_f32 v48, v2, v3
	v_pk_add_f32 v[54:55], v[54:55], 1.0 op_sel_hi:[1,0]
	v_mov_b32_e32 v58, v40
	v_pk_fma_f32 v[4:5], v[54:55], v[50:51], v[4:5]
	ds_write_b128 v199, v[2:5] offset:3072
	v_cvt_pk_fp8_f32 v48, v4, v5 op_sel:[0,0,1]
	v_mov_b32_e32 v59, v42
	v_pk_mul_f32 v[58:59], v[58:59], v[38:39] op_sel_hi:[1,0]
	v_mov_b32_e32 v40, 0
	global_store_dword v[60:61], v48, off offset:768
	global_load_dwordx4 v[2:5], v206, s[0:1]
	s_nop 0
	global_load_dwordx4 v[48:51], v206, s[20:21]
	global_load_dwordx4 v[52:55], v[10:11], off
	v_mov_b32_e32 v56, v44
	v_mov_b32_e32 v57, v46
	v_pk_mul_f32 v[56:57], v[56:57], v[38:39] op_sel_hi:[1,0]
	v_mov_b32_e32 v42, v41
	v_mov_b32_e32 v46, v45
	v_pk_mul_f32 v[44:45], v[46:47], v[38:39] op_sel_hi:[1,0]
	s_waitcnt vmcnt(1)
	v_pk_add_f32 v[48:49], v[48:49], 1.0 op_sel_hi:[1,0]
	s_waitcnt vmcnt(0)
	v_pk_mul_f32 v[52:53], v[58:59], v[52:53]
	v_pk_mul_f32 v[54:55], v[56:57], v[54:55]
	v_pk_fma_f32 v[2:3], v[48:49], v[52:53], v[2:3]
	v_pk_add_f32 v[50:51], v[50:51], 1.0 op_sel_hi:[1,0]
	v_cvt_pk_fp8_f32 v40, v2, v3
	v_pk_fma_f32 v[4:5], v[50:51], v[54:55], v[4:5]
	ds_write_b128 v199, v[2:5] offset:4096
	v_cvt_pk_fp8_f32 v40, v4, v5 op_sel:[0,0,1]
	global_store_dword v[60:61], v40, off offset:1024
	global_load_dwordx4 v[2:5], v207, s[0:1]
	global_load_dwordx4 v[48:51], v207, s[20:21]
	global_load_dwordx4 v[52:55], v[12:13], off
	v_pk_mul_f32 v[40:41], v[42:43], v[38:39] op_sel_hi:[1,0]
	s_waitcnt vmcnt(1)
	v_pk_add_f32 v[46:47], v[48:49], 1.0 op_sel_hi:[1,0]
	s_waitcnt vmcnt(0)
	v_pk_mul_f32 v[40:41], v[40:41], v[52:53]
	v_pk_mul_f32 v[42:43], v[44:45], v[54:55]
	v_pk_fma_f32 v[2:3], v[46:47], v[40:41], v[2:3]
	v_mov_b32_e32 v40, 0
	v_cvt_pk_fp8_f32 v40, v2, v3
	v_pk_add_f32 v[44:45], v[50:51], 1.0 op_sel_hi:[1,0]
	v_mov_b32_e32 v50, v30
	v_pk_fma_f32 v[4:5], v[44:45], v[42:43], v[4:5]
	ds_write_b128 v199, v[2:5] offset:5120
	v_cvt_pk_fp8_f32 v40, v4, v5 op_sel:[0,0,1]
	v_mov_b32_e32 v51, v32
	v_pk_mul_f32 v[50:51], v[50:51], v[38:39] op_sel_hi:[1,0]
	v_mov_b32_e32 v30, 0
	global_store_dword v[60:61], v40, off offset:1280
	global_load_dwordx4 v[2:5], v208, s[0:1]
	s_nop 0
	global_load_dwordx4 v[40:43], v208, s[20:21]
	global_load_dwordx4 v[44:47], v[14:15], off
	v_mov_b32_e32 v48, v34
	v_mov_b32_e32 v49, v36
	v_pk_mul_f32 v[48:49], v[48:49], v[38:39] op_sel_hi:[1,0]
	v_mov_b32_e32 v32, v31
	v_mov_b32_e32 v36, v35
	v_pk_mul_f32 v[34:35], v[36:37], v[38:39] op_sel_hi:[1,0]
	s_waitcnt vmcnt(1)
	v_pk_add_f32 v[40:41], v[40:41], 1.0 op_sel_hi:[1,0]
	s_waitcnt vmcnt(0)
	v_pk_mul_f32 v[44:45], v[50:51], v[44:45]
	v_pk_mul_f32 v[46:47], v[48:49], v[46:47]
	v_pk_fma_f32 v[2:3], v[40:41], v[44:45], v[2:3]
	v_pk_add_f32 v[42:43], v[42:43], 1.0 op_sel_hi:[1,0]
	v_cvt_pk_fp8_f32 v30, v2, v3
	v_pk_fma_f32 v[4:5], v[42:43], v[46:47], v[4:5]
	ds_write_b128 v199, v[2:5] offset:6144
	v_cvt_pk_fp8_f32 v30, v4, v5 op_sel:[0,0,1]
	global_store_dword v[60:61], v30, off offset:1536
	global_load_dwordx4 v[2:5], v209, s[0:1]
	global_load_dwordx4 v[40:43], v209, s[20:21]
	global_load_dwordx4 v[44:47], v[16:17], off
	v_pk_mul_f32 v[30:31], v[32:33], v[38:39] op_sel_hi:[1,0]
	s_add_i32 s0, s22, 1
	s_ashr_i32 s1, s0, 31
	s_lshl_b64 s[20:21], s[0:1], 12
	s_lshl_b64 s[22:23], s[0:1], 11
	s_ashr_i32 s0, s0, 13
	s_mulk_i32 s0, 0x3000
	s_ashr_i32 s1, s0, 31
	s_lshl_b64 s[0:1], s[0:1], 2
	s_waitcnt vmcnt(1)
	v_pk_add_f32 v[36:37], v[40:41], 1.0 op_sel_hi:[1,0]
	s_waitcnt vmcnt(0)
	v_pk_mul_f32 v[30:31], v[30:31], v[44:45]
	v_pk_mul_f32 v[32:33], v[34:35], v[46:47]
	v_pk_fma_f32 v[2:3], v[36:37], v[30:31], v[2:3]
	v_mov_b32_e32 v30, 0
	v_cvt_pk_fp8_f32 v30, v2, v3
	v_pk_add_f32 v[34:35], v[42:43], 1.0 op_sel_hi:[1,0]
	s_nop 0
	v_pk_fma_f32 v[4:5], v[34:35], v[32:33], v[4:5]
	ds_write_b128 v199, v[2:5] offset:7168
	v_cvt_pk_fp8_f32 v30, v4, v5 op_sel:[0,0,1]
	global_store_dword v[60:61], v30, off offset:1792
	v_lshl_add_u64 v[30:31], v[22:23], 0, s[20:21]
	global_load_dwordx2 v[226:227], v[30:31], off offset:2560
	global_load_dwordx2 v[228:229], v[30:31], off offset:3072
	global_load_dwordx2 v[230:231], v[30:31], off offset:3584
	s_add_u32 s20, s3, s0
	s_addc_u32 s21, s24, s1
	s_add_u32 s0, s20, 0x6000
	s_addc_u32 s1, s21, 0
	s_add_u32 s20, s20, 0x8000
	s_addc_u32 s21, s21, 0
	v_and_b32_e32 v3, 0xffff0000, v242
	v_and_b32_e32 v57, 0xffff0000, v244
	v_lshlrev_b32_e32 v2, 16, v242
	v_mul_f32_e32 v34, v3, v3
	v_lshlrev_b32_e32 v56, 16, v244
	v_mul_f32_e32 v32, v57, v57
	v_lshlrev_b32_e32 v4, 16, v243
	v_fmac_f32_e32 v34, v2, v2
	v_lshlrev_b32_e32 v58, 16, v245
	v_fmac_f32_e32 v32, v56, v56
	v_and_b32_e32 v5, 0xffff0000, v243
	v_fmac_f32_e32 v34, v4, v4
	v_and_b32_e32 v59, 0xffff0000, v245
	v_fmac_f32_e32 v32, v58, v58
	v_fmac_f32_e32 v34, v5, v5
	v_fmac_f32_e32 v32, v59, v59
	v_add_f32_e32 v34, v34, v32
	v_and_b32_e32 v53, 0xffff0000, v246
	v_lshlrev_b32_e32 v52, 16, v246
	v_mul_f32_e32 v32, v53, v53
	v_lshlrev_b32_e32 v54, 16, v247
	v_fmac_f32_e32 v32, v52, v52
	v_and_b32_e32 v55, 0xffff0000, v247
	v_fmac_f32_e32 v32, v54, v54
	v_fmac_f32_e32 v32, v55, v55
	v_add_f32_e32 v34, v34, v32
	v_and_b32_e32 v49, 0xffff0000, v248
	v_lshlrev_b32_e32 v48, 16, v248
	v_mul_f32_e32 v32, v49, v49
	v_lshlrev_b32_e32 v50, 16, v249
	v_fmac_f32_e32 v32, v48, v48
	v_and_b32_e32 v51, 0xffff0000, v249
	v_fmac_f32_e32 v32, v50, v50
	v_fmac_f32_e32 v32, v51, v51
	v_add_f32_e32 v36, v34, v32
	v_and_b32_e32 v42, 0xffff0000, v250
	s_waitcnt vmcnt(2)
	v_and_b32_e32 v43, 0xffff0000, v226
	v_lshlrev_b32_e32 v41, 16, v226
	v_lshlrev_b32_e32 v40, 16, v250
	v_lshlrev_b32_e32 v44, 16, v251
	v_and_b32_e32 v46, 0xffff0000, v251
	v_pk_mul_f32 v[32:33], v[42:43], v[42:43]
	v_lshlrev_b32_e32 v45, 16, v227
	v_pk_fma_f32 v[32:33], v[40:41], v[40:41], v[32:33]
	v_and_b32_e32 v47, 0xffff0000, v227
	v_pk_fma_f32 v[32:33], v[44:45], v[44:45], v[32:33]
	s_nop 0
	v_pk_fma_f32 v[32:33], v[46:47], v[46:47], v[32:33]
	s_nop 0
	v_add_f32_e32 v32, v36, v32
	global_load_dwordx4 v[214:217], v202, s[0:1]
	global_load_dwordx4 v[218:221], v202, s[20:21]
	global_load_dwordx4 v[222:225], v[8:9], off
	v_add_f32_e32 v38, v32, v33
	s_waitcnt vmcnt(4)
	v_and_b32_e32 v32, 0xffff0000, v228
	s_waitcnt vmcnt(3)
	v_and_b32_e32 v33, 0xffff0000, v230
	v_lshlrev_b32_e32 v31, 16, v230
	v_lshlrev_b32_e32 v30, 16, v228
	v_lshlrev_b32_e32 v34, 16, v229
	v_and_b32_e32 v36, 0xffff0000, v229
	v_pk_mul_f32 v[60:61], v[32:33], v[32:33]
	v_lshlrev_b32_e32 v35, 16, v231
	v_pk_fma_f32 v[60:61], v[30:31], v[30:31], v[60:61]
	v_and_b32_e32 v37, 0xffff0000, v231
	v_pk_fma_f32 v[60:61], v[34:35], v[34:35], v[60:61]
	s_waitcnt vmcnt(1)
	v_pk_add_f32 v[218:219], v[218:219], 1.0 op_sel_hi:[1,0]
	v_pk_fma_f32 v[60:61], v[36:37], v[36:37], v[60:61]
	s_nop 0
	v_add_f32_e32 v38, v38, v60
	v_add_f32_e32 v38, v38, v61
	ds_bpermute_b32 v60, v189, v38
	s_waitcnt lgkmcnt(0)
	v_add_f32_e32 v38, v38, v60
	ds_bpermute_b32 v60, v192, v38
	s_waitcnt lgkmcnt(0)
	v_add_f32_e32 v38, v38, v60
	ds_bpermute_b32 v60, v193, v38
	s_waitcnt lgkmcnt(0)
	v_add_f32_e32 v38, v38, v60
	ds_bpermute_b32 v60, v194, v38
	s_waitcnt lgkmcnt(0)
	v_add_f32_e32 v38, v38, v60
	ds_bpermute_b32 v60, v195, v38
	s_waitcnt lgkmcnt(0)
	v_add_f32_e32 v38, v38, v60
	ds_bpermute_b32 v60, v196, v38
	s_waitcnt lgkmcnt(0)
	v_add_f32_e32 v38, v38, v60
	v_fmamk_f32 v38, v38, 0x3a000000, v201
	v_cmp_gt_f32_e32 vcc, s27, v38
	v_mul_f32_e32 v60, 0x4b800000, v38
	s_nop 0
	v_cndmask_b32_e32 v38, v38, v60, vcc
	v_rsq_f32_e32 v38, v38
	s_nop 0
	v_mul_f32_e32 v60, 0x45800000, v38
	v_cndmask_b32_e32 v38, v38, v60, vcc
	v_pk_mul_f32 v[2:3], v[2:3], v[38:39] op_sel_hi:[1,0]
	v_pk_mul_f32 v[4:5], v[4:5], v[38:39] op_sel_hi:[1,0]
	s_waitcnt vmcnt(0)
	v_pk_mul_f32 v[2:3], v[222:223], v[2:3]
	v_pk_mul_f32 v[4:5], v[224:225], v[4:5]
	v_pk_fma_f32 v[2:3], v[218:219], v[2:3], v[214:215]
	v_mov_b32_e32 v214, 0
	v_cvt_pk_fp8_f32 v214, v2, v3
	v_pk_add_f32 v[60:61], v[220:221], 1.0 op_sel_hi:[1,0]
	v_pk_mul_f32 v[56:57], v[56:57], v[38:39] op_sel_hi:[1,0]
	v_pk_fma_f32 v[4:5], v[60:61], v[4:5], v[216:217]
	v_lshl_add_u64 v[60:61], v[24:25], 0, s[22:23]
	v_cvt_pk_fp8_f32 v214, v4, v5 op_sel:[0,0,1]
	ds_write_b128 v200, v[2:5]
	v_pk_mul_f32 v[58:59], v[58:59], v[38:39] op_sel_hi:[1,0]
	v_pk_mul_f32 v[52:53], v[52:53], v[38:39] op_sel_hi:[1,0]
	global_store_dword v[60:61], v214, off
	global_load_dwordx4 v[2:5], v203, s[0:1]
	s_nop 0
	global_load_dwordx4 v[214:217], v203, s[20:21]
	global_load_dwordx4 v[218:221], v[8:9], off offset:1024
	v_pk_mul_f32 v[54:55], v[54:55], v[38:39] op_sel_hi:[1,0]
	v_pk_mul_f32 v[48:49], v[48:49], v[38:39] op_sel_hi:[1,0]
	v_pk_mul_f32 v[50:51], v[50:51], v[38:39] op_sel_hi:[1,0]
	s_waitcnt vmcnt(1)
	v_pk_add_f32 v[214:215], v[214:215], 1.0 op_sel_hi:[1,0]
	s_waitcnt vmcnt(0)
	v_pk_mul_f32 v[56:57], v[218:219], v[56:57]
	v_pk_mul_f32 v[58:59], v[220:221], v[58:59]
	v_pk_fma_f32 v[2:3], v[214:215], v[56:57], v[2:3]
	v_mov_b32_e32 v56, 0
	v_cvt_pk_fp8_f32 v56, v2, v3
	v_pk_add_f32 v[216:217], v[216:217], 1.0 op_sel_hi:[1,0]
	s_nop 0
	v_pk_fma_f32 v[4:5], v[216:217], v[58:59], v[4:5]
	ds_write_b128 v200, v[2:5] offset:1024
	v_cvt_pk_fp8_f32 v56, v4, v5 op_sel:[0,0,1]
	global_store_dword v[60:61], v56, off offset:256
	global_load_dwordx4 v[2:5], v204, s[0:1]
	s_nop 0
	global_load_dwordx4 v[56:59], v204, s[20:21]
	global_load_dwordx4 v[214:217], v[8:9], off offset:2048
	s_waitcnt vmcnt(1)
	v_pk_add_f32 v[56:57], v[56:57], 1.0 op_sel_hi:[1,0]
	s_waitcnt vmcnt(0)
	v_pk_mul_f32 v[52:53], v[214:215], v[52:53]
	v_pk_mul_f32 v[54:55], v[216:217], v[54:55]
	v_pk_fma_f32 v[2:3], v[56:57], v[52:53], v[2:3]
	v_mov_b32_e32 v52, 0
	v_cvt_pk_fp8_f32 v52, v2, v3
	v_pk_add_f32 v[58:59], v[58:59], 1.0 op_sel_hi:[1,0]
	s_nop 0
	v_pk_fma_f32 v[4:5], v[58:59], v[54:55], v[4:5]
	ds_write_b128 v200, v[2:5] offset:2048
	v_cvt_pk_fp8_f32 v52, v4, v5 op_sel:[0,0,1]
	global_store_dword v[60:61], v52, off offset:512
	global_load_dwordx4 v[2:5], v205, s[0:1]
	s_nop 0
	global_load_dwordx4 v[52:55], v205, s[20:21]
	global_load_dwordx4 v[56:59], v[8:9], off offset:3072
	s_waitcnt vmcnt(1)
	v_pk_add_f32 v[52:53], v[52:53], 1.0 op_sel_hi:[1,0]
	s_waitcnt vmcnt(0)
	v_pk_mul_f32 v[48:49], v[48:49], v[56:57]
	v_pk_mul_f32 v[50:51], v[50:51], v[58:59]
	v_pk_fma_f32 v[2:3], v[52:53], v[48:49], v[2:3]
	v_mov_b32_e32 v48, 0
	v_cvt_pk_fp8_f32 v48, v2, v3
	v_pk_add_f32 v[54:55], v[54:55], 1.0 op_sel_hi:[1,0]
	v_mov_b32_e32 v58, v40
	v_pk_fma_f32 v[4:5], v[54:55], v[50:51], v[4:5]
	ds_write_b128 v200, v[2:5] offset:3072
	v_cvt_pk_fp8_f32 v48, v4, v5 op_sel:[0,0,1]
	v_mov_b32_e32 v59, v42
	v_pk_mul_f32 v[58:59], v[58:59], v[38:39] op_sel_hi:[1,0]
	v_mov_b32_e32 v40, 0
	global_store_dword v[60:61], v48, off offset:768
	global_load_dwordx4 v[2:5], v206, s[0:1]
	s_nop 0
	global_load_dwordx4 v[48:51], v206, s[20:21]
	global_load_dwordx4 v[52:55], v[10:11], off
	v_mov_b32_e32 v56, v44
	v_mov_b32_e32 v57, v46
	v_pk_mul_f32 v[56:57], v[56:57], v[38:39] op_sel_hi:[1,0]
	v_mov_b32_e32 v42, v41
	v_mov_b32_e32 v46, v45
	v_pk_mul_f32 v[44:45], v[46:47], v[38:39] op_sel_hi:[1,0]
	s_waitcnt vmcnt(1)
	v_pk_add_f32 v[48:49], v[48:49], 1.0 op_sel_hi:[1,0]
	s_waitcnt vmcnt(0)
	v_pk_mul_f32 v[52:53], v[58:59], v[52:53]
	v_pk_mul_f32 v[54:55], v[56:57], v[54:55]
	v_pk_fma_f32 v[2:3], v[48:49], v[52:53], v[2:3]
	v_pk_add_f32 v[50:51], v[50:51], 1.0 op_sel_hi:[1,0]
	v_cvt_pk_fp8_f32 v40, v2, v3
	v_pk_fma_f32 v[4:5], v[50:51], v[54:55], v[4:5]
	ds_write_b128 v200, v[2:5] offset:4096
	v_cvt_pk_fp8_f32 v40, v4, v5 op_sel:[0,0,1]
	global_store_dword v[60:61], v40, off offset:1024
	global_load_dwordx4 v[2:5], v207, s[0:1]
	global_load_dwordx4 v[48:51], v207, s[20:21]
	global_load_dwordx4 v[52:55], v[12:13], off
	v_pk_mul_f32 v[40:41], v[42:43], v[38:39] op_sel_hi:[1,0]
	s_waitcnt vmcnt(1)
	v_pk_add_f32 v[46:47], v[48:49], 1.0 op_sel_hi:[1,0]
	s_waitcnt vmcnt(0)
	v_pk_mul_f32 v[40:41], v[40:41], v[52:53]
	v_pk_mul_f32 v[42:43], v[44:45], v[54:55]
	v_pk_fma_f32 v[2:3], v[46:47], v[40:41], v[2:3]
	v_mov_b32_e32 v40, 0
	v_cvt_pk_fp8_f32 v40, v2, v3
	v_pk_add_f32 v[44:45], v[50:51], 1.0 op_sel_hi:[1,0]
	v_mov_b32_e32 v50, v30
	v_pk_fma_f32 v[4:5], v[44:45], v[42:43], v[4:5]
	ds_write_b128 v200, v[2:5] offset:5120
	v_cvt_pk_fp8_f32 v40, v4, v5 op_sel:[0,0,1]
	v_mov_b32_e32 v51, v32
	v_pk_mul_f32 v[50:51], v[50:51], v[38:39] op_sel_hi:[1,0]
	v_mov_b32_e32 v30, 0
	global_store_dword v[60:61], v40, off offset:1280
	global_load_dwordx4 v[2:5], v208, s[0:1]
	s_nop 0
	global_load_dwordx4 v[40:43], v208, s[20:21]
	global_load_dwordx4 v[44:47], v[14:15], off
	v_mov_b32_e32 v48, v34
	v_mov_b32_e32 v49, v36
	v_pk_mul_f32 v[48:49], v[48:49], v[38:39] op_sel_hi:[1,0]
	v_mov_b32_e32 v32, v31
	v_mov_b32_e32 v36, v35
	v_pk_mul_f32 v[34:35], v[36:37], v[38:39] op_sel_hi:[1,0]
	s_waitcnt vmcnt(1)
	v_pk_add_f32 v[40:41], v[40:41], 1.0 op_sel_hi:[1,0]
	s_waitcnt vmcnt(0)
	v_pk_mul_f32 v[44:45], v[50:51], v[44:45]
	v_pk_mul_f32 v[46:47], v[48:49], v[46:47]
	v_pk_fma_f32 v[2:3], v[40:41], v[44:45], v[2:3]
	v_pk_add_f32 v[42:43], v[42:43], 1.0 op_sel_hi:[1,0]
	v_cvt_pk_fp8_f32 v30, v2, v3
	v_pk_fma_f32 v[4:5], v[42:43], v[46:47], v[4:5]
	ds_write_b128 v200, v[2:5] offset:6144
	v_cvt_pk_fp8_f32 v30, v4, v5 op_sel:[0,0,1]
	global_store_dword v[60:61], v30, off offset:1536
	global_load_dwordx4 v[2:5], v209, s[0:1]
	global_load_dwordx4 v[40:43], v209, s[20:21]
	global_load_dwordx4 v[44:47], v[16:17], off
	v_pk_mul_f32 v[30:31], v[32:33], v[38:39] op_sel_hi:[1,0]
	s_waitcnt vmcnt(1)
	v_pk_add_f32 v[36:37], v[40:41], 1.0 op_sel_hi:[1,0]
	s_waitcnt vmcnt(0)
	v_pk_mul_f32 v[30:31], v[30:31], v[44:45]
	v_pk_mul_f32 v[32:33], v[34:35], v[46:47]
	v_pk_fma_f32 v[2:3], v[36:37], v[30:31], v[2:3]
	v_mov_b32_e32 v30, 0
	v_cvt_pk_fp8_f32 v30, v2, v3
	v_pk_add_f32 v[34:35], v[42:43], 1.0 op_sel_hi:[1,0]
	s_nop 0
	v_pk_fma_f32 v[4:5], v[34:35], v[32:33], v[4:5]
	ds_write_b128 v200, v[2:5] offset:7168
	v_cvt_pk_fp8_f32 v30, v4, v5 op_sel:[0,0,1]
	global_store_dword v[60:61], v30, off offset:1792
	s_waitcnt lgkmcnt(0)
	s_barrier
	ds_read_b128 v[2:5], v210
	s_waitcnt lgkmcnt(0)
	v_mfma_f32_16x16x4_f32 v[30:33], v2, v1, 0
	v_mfma_f32_16x16x4_f32 v[34:37], v2, v39, 0
	v_mfma_f32_16x16x4_f32 v[30:33], v3, v62, v[30:33]
	v_mfma_f32_16x16x4_f32 v[34:37], v3, v63, v[34:37]
	v_mfma_f32_16x16x4_f32 v[30:33], v4, v64, v[30:33]
	v_mfma_f32_16x16x4_f32 v[34:37], v4, v65, v[34:37]
	v_mfma_f32_16x16x4_f32 v[30:33], v5, v66, v[30:33]
	v_mfma_f32_16x16x4_f32 v[2:5], v5, v67, v[34:37]
	s_nop 7
	ds_read_b128 v[34:37], v210 offset:64
	s_waitcnt lgkmcnt(0)
	v_mfma_f32_16x16x4_f32 v[30:33], v34, v68, v[30:33]
	v_mfma_f32_16x16x4_f32 v[2:5], v34, v69, v[2:5]
	v_mfma_f32_16x16x4_f32 v[30:33], v35, v70, v[30:33]
	v_mfma_f32_16x16x4_f32 v[2:5], v35, v71, v[2:5]
	v_mfma_f32_16x16x4_f32 v[30:33], v36, v72, v[30:33]
	v_mfma_f32_16x16x4_f32 v[2:5], v36, v73, v[2:5]
	v_mfma_f32_16x16x4_f32 v[30:33], v37, v74, v[30:33]
	v_mfma_f32_16x16x4_f32 v[2:5], v37, v75, v[2:5]
	ds_read_b128 v[34:37], v210 offset:128
	s_waitcnt lgkmcnt(0)
	v_mfma_f32_16x16x4_f32 v[30:33], v34, v76, v[30:33]
	v_mfma_f32_16x16x4_f32 v[2:5], v34, v77, v[2:5]
	v_mfma_f32_16x16x4_f32 v[30:33], v35, v78, v[30:33]
	v_mfma_f32_16x16x4_f32 v[2:5], v35, v79, v[2:5]
	v_mfma_f32_16x16x4_f32 v[30:33], v36, v80, v[30:33]
	v_mfma_f32_16x16x4_f32 v[2:5], v36, v81, v[2:5]
	v_mfma_f32_16x16x4_f32 v[30:33], v37, v82, v[30:33]
	v_mfma_f32_16x16x4_f32 v[2:5], v37, v83, v[2:5]
	ds_read_b128 v[34:37], v210 offset:192
	s_waitcnt lgkmcnt(0)
	v_mfma_f32_16x16x4_f32 v[30:33], v34, v84, v[30:33]
	v_mfma_f32_16x16x4_f32 v[2:5], v34, v85, v[2:5]
	v_mfma_f32_16x16x4_f32 v[30:33], v35, v86, v[30:33]
	v_mfma_f32_16x16x4_f32 v[2:5], v35, v87, v[2:5]
	v_mfma_f32_16x16x4_f32 v[30:33], v36, v88, v[30:33]
	v_mfma_f32_16x16x4_f32 v[2:5], v36, v89, v[2:5]
	v_mfma_f32_16x16x4_f32 v[30:33], v37, v90, v[30:33]
	v_mfma_f32_16x16x4_f32 v[2:5], v37, v91, v[2:5]
	ds_read_b128 v[34:37], v210 offset:256
	s_waitcnt lgkmcnt(0)
	v_mfma_f32_16x16x4_f32 v[30:33], v34, v92, v[30:33]
	v_mfma_f32_16x16x4_f32 v[2:5], v34, v93, v[2:5]
	v_mfma_f32_16x16x4_f32 v[30:33], v35, v94, v[30:33]
	v_mfma_f32_16x16x4_f32 v[2:5], v35, v95, v[2:5]
	v_mfma_f32_16x16x4_f32 v[30:33], v36, v96, v[30:33]
	v_mfma_f32_16x16x4_f32 v[2:5], v36, v97, v[2:5]
	v_mfma_f32_16x16x4_f32 v[30:33], v37, v98, v[30:33]
	v_mfma_f32_16x16x4_f32 v[2:5], v37, v99, v[2:5]
	ds_read_b128 v[34:37], v210 offset:320
	s_waitcnt lgkmcnt(0)
	v_mfma_f32_16x16x4_f32 v[30:33], v34, v100, v[30:33]
	v_mfma_f32_16x16x4_f32 v[2:5], v34, v101, v[2:5]
	v_mfma_f32_16x16x4_f32 v[30:33], v35, v102, v[30:33]
	v_mfma_f32_16x16x4_f32 v[2:5], v35, v103, v[2:5]
	v_mfma_f32_16x16x4_f32 v[30:33], v36, v104, v[30:33]
	v_mfma_f32_16x16x4_f32 v[2:5], v36, v105, v[2:5]
	v_mfma_f32_16x16x4_f32 v[30:33], v37, v106, v[30:33]
	v_mfma_f32_16x16x4_f32 v[2:5], v37, v107, v[2:5]
	ds_read_b128 v[34:37], v210 offset:384
	s_waitcnt lgkmcnt(0)
	v_mfma_f32_16x16x4_f32 v[30:33], v34, v108, v[30:33]
	v_mfma_f32_16x16x4_f32 v[2:5], v34, v109, v[2:5]
	v_mfma_f32_16x16x4_f32 v[30:33], v35, v110, v[30:33]
	v_mfma_f32_16x16x4_f32 v[2:5], v35, v111, v[2:5]
	v_mfma_f32_16x16x4_f32 v[30:33], v36, v112, v[30:33]
	v_mfma_f32_16x16x4_f32 v[2:5], v36, v113, v[2:5]
	v_mfma_f32_16x16x4_f32 v[30:33], v37, v114, v[30:33]
	v_mfma_f32_16x16x4_f32 v[2:5], v37, v115, v[2:5]
	ds_read_b128 v[34:37], v210 offset:448
	s_waitcnt lgkmcnt(0)
	v_mfma_f32_16x16x4_f32 v[30:33], v34, v116, v[30:33]
	v_mfma_f32_16x16x4_f32 v[2:5], v34, v117, v[2:5]
	v_mfma_f32_16x16x4_f32 v[30:33], v35, v118, v[30:33]
	v_mfma_f32_16x16x4_f32 v[2:5], v35, v119, v[2:5]
	v_mfma_f32_16x16x4_f32 v[30:33], v36, v120, v[30:33]
	v_mfma_f32_16x16x4_f32 v[2:5], v36, v121, v[2:5]
	v_mfma_f32_16x16x4_f32 v[30:33], v37, v122, v[30:33]
	v_mfma_f32_16x16x4_f32 v[2:5], v37, v123, v[2:5]
	ds_read_b128 v[34:37], v210 offset:512
	s_waitcnt lgkmcnt(0)
	v_mfma_f32_16x16x4_f32 v[30:33], v34, v124, v[30:33]
	v_mfma_f32_16x16x4_f32 v[2:5], v34, v125, v[2:5]
	v_mfma_f32_16x16x4_f32 v[30:33], v35, v126, v[30:33]
	v_mfma_f32_16x16x4_f32 v[2:5], v35, v127, v[2:5]
	v_mfma_f32_16x16x4_f32 v[30:33], v36, v128, v[30:33]
	v_mfma_f32_16x16x4_f32 v[2:5], v36, v129, v[2:5]
	v_mfma_f32_16x16x4_f32 v[30:33], v37, v130, v[30:33]
	v_mfma_f32_16x16x4_f32 v[2:5], v37, v131, v[2:5]
	ds_read_b128 v[34:37], v210 offset:576
	s_waitcnt lgkmcnt(0)
	v_mfma_f32_16x16x4_f32 v[30:33], v34, v132, v[30:33]
	v_mfma_f32_16x16x4_f32 v[2:5], v34, v133, v[2:5]
	v_mfma_f32_16x16x4_f32 v[30:33], v35, v134, v[30:33]
	v_mfma_f32_16x16x4_f32 v[2:5], v35, v135, v[2:5]
	v_mfma_f32_16x16x4_f32 v[30:33], v36, v136, v[30:33]
	v_mfma_f32_16x16x4_f32 v[2:5], v36, v137, v[2:5]
	v_mfma_f32_16x16x4_f32 v[30:33], v37, v138, v[30:33]
	v_mfma_f32_16x16x4_f32 v[2:5], v37, v139, v[2:5]
	ds_read_b128 v[34:37], v210 offset:640
	s_waitcnt lgkmcnt(0)
	v_mfma_f32_16x16x4_f32 v[30:33], v34, v140, v[30:33]
	v_mfma_f32_16x16x4_f32 v[2:5], v34, v141, v[2:5]
	v_mfma_f32_16x16x4_f32 v[30:33], v35, v142, v[30:33]
	v_mfma_f32_16x16x4_f32 v[2:5], v35, v143, v[2:5]
	v_mfma_f32_16x16x4_f32 v[30:33], v36, v144, v[30:33]
	v_mfma_f32_16x16x4_f32 v[2:5], v36, v145, v[2:5]
	v_mfma_f32_16x16x4_f32 v[30:33], v37, v146, v[30:33]
	v_mfma_f32_16x16x4_f32 v[2:5], v37, v147, v[2:5]
	ds_read_b128 v[34:37], v210 offset:704
	s_waitcnt lgkmcnt(0)
	v_mfma_f32_16x16x4_f32 v[30:33], v34, v148, v[30:33]
	v_mfma_f32_16x16x4_f32 v[2:5], v34, v149, v[2:5]
	v_mfma_f32_16x16x4_f32 v[30:33], v35, v150, v[30:33]
	v_mfma_f32_16x16x4_f32 v[2:5], v35, v151, v[2:5]
	v_mfma_f32_16x16x4_f32 v[30:33], v36, v152, v[30:33]
	v_mfma_f32_16x16x4_f32 v[2:5], v36, v153, v[2:5]
	v_mfma_f32_16x16x4_f32 v[30:33], v37, v154, v[30:33]
	v_mfma_f32_16x16x4_f32 v[2:5], v37, v155, v[2:5]
	ds_read_b128 v[34:37], v210 offset:768
	s_waitcnt lgkmcnt(0)
	v_mfma_f32_16x16x4_f32 v[30:33], v34, v156, v[30:33]
	v_mfma_f32_16x16x4_f32 v[2:5], v34, v157, v[2:5]
	v_mfma_f32_16x16x4_f32 v[30:33], v35, v158, v[30:33]
	v_mfma_f32_16x16x4_f32 v[2:5], v35, v159, v[2:5]
	v_mfma_f32_16x16x4_f32 v[30:33], v36, v160, v[30:33]
	v_mfma_f32_16x16x4_f32 v[2:5], v36, v161, v[2:5]
	v_mfma_f32_16x16x4_f32 v[30:33], v37, v162, v[30:33]
	v_mfma_f32_16x16x4_f32 v[2:5], v37, v163, v[2:5]
	ds_read_b128 v[34:37], v210 offset:832
	s_waitcnt lgkmcnt(0)
	v_mfma_f32_16x16x4_f32 v[30:33], v34, v164, v[30:33]
	v_mfma_f32_16x16x4_f32 v[2:5], v34, v165, v[2:5]
	v_mfma_f32_16x16x4_f32 v[30:33], v35, v166, v[30:33]
	v_mfma_f32_16x16x4_f32 v[2:5], v35, v167, v[2:5]
	v_mfma_f32_16x16x4_f32 v[30:33], v36, v168, v[30:33]
	v_mfma_f32_16x16x4_f32 v[2:5], v36, v169, v[2:5]
	v_mfma_f32_16x16x4_f32 v[30:33], v37, v170, v[30:33]
	v_mfma_f32_16x16x4_f32 v[2:5], v37, v171, v[2:5]
	ds_read_b128 v[34:37], v210 offset:896
	s_waitcnt lgkmcnt(0)
	v_mfma_f32_16x16x4_f32 v[30:33], v34, v172, v[30:33]
	v_mfma_f32_16x16x4_f32 v[2:5], v34, v173, v[2:5]
	v_mfma_f32_16x16x4_f32 v[30:33], v35, v174, v[30:33]
	v_mfma_f32_16x16x4_f32 v[2:5], v35, v175, v[2:5]
	v_mfma_f32_16x16x4_f32 v[30:33], v36, v176, v[30:33]
	v_mfma_f32_16x16x4_f32 v[2:5], v36, v177, v[2:5]
	v_mfma_f32_16x16x4_f32 v[30:33], v37, v178, v[30:33]
	v_mfma_f32_16x16x4_f32 v[2:5], v37, v179, v[2:5]
	ds_read_b128 v[34:37], v210 offset:960
	s_waitcnt lgkmcnt(0)
	v_mfma_f32_16x16x4_f32 v[30:33], v34, v180, v[30:33]
	v_mfma_f32_16x16x4_f32 v[2:5], v34, v181, v[2:5]
	v_mfma_f32_16x16x4_f32 v[30:33], v35, v182, v[30:33]
	v_mfma_f32_16x16x4_f32 v[2:5], v35, v183, v[2:5]
	v_mfma_f32_16x16x4_f32 v[30:33], v36, v184, v[30:33]
	v_mfma_f32_16x16x4_f32 v[2:5], v36, v185, v[2:5]
	v_mfma_f32_16x16x4_f32 v[30:33], v37, v186, v[30:33]
	v_mfma_f32_16x16x4_f32 v[2:5], v37, v187, v[2:5]
	s_nop 9
	ds_write2_b32 v211, v30, v2 offset1:16
	ds_write2_b32 v211, v31, v3 offset0:32 offset1:48
	ds_write2_b32 v211, v32, v4 offset0:64 offset1:80
	ds_write2_b32 v211, v33, v5 offset0:96 offset1:112
	s_waitcnt lgkmcnt(0)
	s_barrier
	global_load_dword v4, v[18:19], off
	ds_read2st64_b32 v[2:3], v198 offset1:8
	ds_bpermute_b32 v31, v192, v197
	s_waitcnt vmcnt(0) lgkmcnt(1)
	v_add_f32_e32 v2, v4, v2
	v_add_f32_e32 v4, v2, v3
	ds_read2st64_b32 v[2:3], v198 offset0:16 offset1:24
	s_waitcnt lgkmcnt(0)
	v_add_f32_e32 v2, v4, v2
	v_add_f32_e32 v4, v2, v3
	ds_read2st64_b32 v[2:3], v198 offset0:32 offset1:40
	s_waitcnt lgkmcnt(0)
	v_add_f32_e32 v2, v4, v2
	v_add_f32_e32 v4, v2, v3
	ds_read2st64_b32 v[2:3], v198 offset0:48 offset1:56
	s_waitcnt lgkmcnt(0)
	v_add_f32_e32 v2, v4, v2
	v_add_f32_e32 v3, v2, v3
	ds_bpermute_b32 v5, v192, v3
	s_waitcnt lgkmcnt(0)
	v_cmp_lt_f32_e64 s[20:21], v3, v5
	v_cmp_nlt_f32_e32 vcc, v3, v5
	s_and_saveexec_b64 s[22:23], vcc
	v_cmp_eq_f32_e32 vcc, v3, v5
	v_cmp_lt_i32_e64 s[0:1], v31, v197
	s_and_b64 s[0:1], vcc, s[0:1]
	s_andn2_b64 s[20:21], s[20:21], exec
	s_and_b64 s[0:1], s[0:1], exec
	s_or_b64 s[20:21], s[20:21], s[0:1]
	s_or_b64 exec, exec, s[22:23]
	v_mov_b32_e32 v4, v3
	v_mov_b32_e32 v30, v3
	v_mov_b32_e32 v2, v197
	s_and_saveexec_b64 s[0:1], s[20:21]
	v_mov_b32_e32 v4, v5
	v_mov_b32_e32 v30, v5
	v_mov_b32_e32 v2, v31
	s_or_b64 exec, exec, s[0:1]
	ds_bpermute_b32 v5, v193, v4
	ds_bpermute_b32 v31, v193, v2
	s_waitcnt lgkmcnt(1)
	v_cmp_lt_f32_e64 s[20:21], v30, v5
	v_cmp_nlt_f32_e32 vcc, v30, v5
	s_and_saveexec_b64 s[22:23], vcc
	s_cbranch_execz .LBB0_688
	v_cmp_eq_f32_e32 vcc, v30, v5
	s_waitcnt lgkmcnt(0)
	v_cmp_lt_i32_e64 s[0:1], v31, v2
	s_and_b64 s[0:1], vcc, s[0:1]
	s_andn2_b64 s[20:21], s[20:21], exec
	s_and_b64 s[0:1], s[0:1], exec
	s_or_b64 s[20:21], s[20:21], s[0:1]

	.amdhsa_kernel _Z3fwd6Params
		.amdhsa_group_segment_fixed_size 0
		.amdhsa_private_segment_fixed_size 0
		.amdhsa_kernarg_size 432
		.amdhsa_user_sgpr_count 2
		.amdhsa_user_sgpr_dispatch_ptr 0
		.amdhsa_user_sgpr_queue_ptr 0
		.amdhsa_user_sgpr_kernarg_segment_ptr 1
		.amdhsa_user_sgpr_dispatch_id 0
		.amdhsa_user_sgpr_kernarg_preload_length 0
		.amdhsa_user_sgpr_kernarg_preload_offset 0
		.amdhsa_user_sgpr_private_segment_size 0
		.amdhsa_uses_dynamic_stack 0
		.amdhsa_enable_private_segment 0
		.amdhsa_system_sgpr_workgroup_id_x 1
		.amdhsa_system_sgpr_workgroup_id_y 0
		.amdhsa_system_sgpr_workgroup_id_z 0
		.amdhsa_system_sgpr_workgroup_info 0
		.amdhsa_system_vgpr_workitem_id 0
		.amdhsa_next_free_vgpr 255
		.amdhsa_next_free_sgpr 100
		.amdhsa_accum_offset 256
		.amdhsa_reserve_vcc 1
		.amdhsa_float_round_mode_32 0
		.amdhsa_float_round_mode_16_64 0
		.amdhsa_float_denorm_mode_32 3
		.amdhsa_float_denorm_mode_16_64 3
		.amdhsa_dx10_clamp 1
		.amdhsa_ieee_mode 1
		.amdhsa_fp16_overflow 0
		.amdhsa_tg_split 0
		.amdhsa_exception_fp_ieee_invalid_op 0
		.amdhsa_exception_fp_denorm_src 0
		.amdhsa_exception_fp_ieee_div_zero 0
		.amdhsa_exception_fp_ieee_overflow 0
		.amdhsa_exception_fp_ieee_underflow 0
		.amdhsa_exception_fp_ieee_inexact 0
		.amdhsa_exception_int_div_zero 0
	.end_amdhsa_kernel

amdhsa.kernels:
  - .agpr_count:     0
    .args:
      - .offset:         0
        .size:           176
        .value_kind:     by_value
      - .offset:         176
        .size:           4
        .value_kind:     hidden_block_count_x
      - .offset:         180
        .size:           4
        .value_kind:     hidden_block_count_y
      - .offset:         184
        .size:           4
        .value_kind:     hidden_block_count_z
      - .offset:         188
        .size:           2
        .value_kind:     hidden_group_size_x
      - .offset:         190
        .size:           2
        .value_kind:     hidden_group_size_y
      - .offset:         192
        .size:           2
        .value_kind:     hidden_group_size_z
      - .offset:         194
        .size:           2
        .value_kind:     hidden_remainder_x
      - .offset:         196
        .size:           2
        .value_kind:     hidden_remainder_y
      - .offset:         198
        .size:           2
        .value_kind:     hidden_remainder_z
      - .offset:         216
        .size:           8
        .value_kind:     hidden_global_offset_x
      - .offset:         224
        .size:           8
        .value_kind:     hidden_global_offset_y
      - .offset:         232
        .size:           8
        .value_kind:     hidden_global_offset_z
      - .offset:         240
        .size:           2
        .value_kind:     hidden_grid_dims
      - .offset:         296
        .size:           4
        .value_kind:     hidden_dynamic_lds_size
    .group_segment_fixed_size: 0
    .kernarg_segment_align: 8
    .kernarg_segment_size: 432
    .language:       OpenCL C
    .language_version:
      - 2
      - 0
    .max_flat_workgroup_size: 512
    .name:           _Z3fwd6Params
    .private_segment_fixed_size: 0
    .sgpr_count:     106
    .sgpr_spill_count: 13
    .symbol:         _Z3fwd6Params.kd
    .uniform_work_group_size: 1
    .uses_dynamic_stack: false
    .vgpr_count:     255
    .vgpr_spill_count: 0
    .wavefront_size: 64
